# P8 K-loop: each load segment issues its LDS-DMA group right after the opening barrier, ahead of the fragment ds_reads (longer window before the counted wait); on v54
# baseline (speedup 1.0000x reference)
.LBB0_889:
	v_mov_b32_e32 v223, v3
	s_waitcnt lgkmcnt(0)
	v_lshl_add_u64 v[36:37], s[48:49], 0, v[2:3]
	v_lshl_add_u64 v[38:39], s[48:49], 0, v[222:223]
	v_cndmask_b32_e64 v2, v206, v229, s[40:41]
	v_cndmask_b32_e64 v64, v210, v231, s[40:41]
	s_setprio 0
	s_barrier
	s_mov_b32 m0, s61
	s_nop 0
	global_load_lds_dwordx4 v2, s[48:49]
	s_mov_b32 m0, s62
	s_nop 0
	global_load_lds_dwordx4 v64, s[48:49]
	s_add_i32 s40, 0, 0x18000
	s_add_i32 s41, 0, 0x1c000
	v_add_u32_e32 v4, s40, v226
	v_add_u32_e32 v16, s41, v226
	ds_read_b128 v[20:23], v4
	ds_read_b128 v[24:27], v4 offset:1024
	ds_read_b128 v[28:31], v4 offset:2048
	ds_read_b128 v[32:35], v4 offset:3072
	ds_read_b128 v[4:7], v16
	ds_read_b128 v[8:11], v16 offset:1024
	ds_read_b128 v[12:15], v16 offset:2048
	ds_read_b128 v[16:19], v16 offset:3072
	ds_read_b128 v[40:43], v227 offset:32768
	ds_read_b128 v[44:47], v227 offset:33792
	ds_read_b128 v[48:51], v227 offset:34816
	ds_read_b128 v[52:55], v227 offset:35840
	ds_read_b128 v[56:59], v227 offset:36864
	ds_read_b128 v[60:63], v227 offset:37888
	ds_read_b128 v[232:235], v227 offset:38912
	ds_read_b128 v[236:239], v227 offset:39936
	s_waitcnt vmcnt(8)
	s_waitcnt lgkmcnt(0)
	s_barrier
	s_setprio 1
	s_waitcnt lgkmcnt(0)
	v_mfma_scale_f32_16x16x128_f8f6f4 v[80:83], v[20:27], v[40:47], v[80:83], v224, v149 op_sel_hi:[0,0,0]
	v_mfma_scale_f32_16x16x128_f8f6f4 v[88:91], v[28:35], v[40:47], v[88:91], v224, v149 op_sel_hi:[0,0,0]
	v_mfma_scale_f32_16x16x128_f8f6f4 v[96:99], v[20:27], v[48:55], v[96:99], v224, v149 op_sel_hi:[0,0,0]
	v_mfma_scale_f32_16x16x128_f8f6f4 v[104:107], v[28:35], v[48:55], v[104:107], v224, v149 op_sel_hi:[0,0,0]
	v_mfma_scale_f32_16x16x128_f8f6f4 v[112:115], v[20:27], v[56:63], v[112:115], v224, v149 op_sel_hi:[0,0,0]
	v_mfma_scale_f32_16x16x128_f8f6f4 v[120:123], v[28:35], v[56:63], v[120:123], v224, v149 op_sel_hi:[0,0,0]
	v_mfma_scale_f32_16x16x128_f8f6f4 v[128:131], v[20:27], v[232:239], v[128:131], v224, v149 op_sel_hi:[0,0,0]
	v_mfma_scale_f32_16x16x128_f8f6f4 v[132:135], v[28:35], v[232:239], v[132:135], v224, v149 op_sel_hi:[0,0,0]
	s_setprio 0
	s_setprio 1
	v_mfma_scale_f32_16x16x128_f8f6f4 v[144:147], v[4:11], v[40:47], v[144:147], v224, v149 op_sel_hi:[0,0,0]
	v_mfma_scale_f32_16x16x128_f8f6f4 v[154:157], v[12:19], v[40:47], v[154:157], v224, v149 op_sel_hi:[0,0,0]
	v_mfma_scale_f32_16x16x128_f8f6f4 v[158:161], v[4:11], v[48:55], v[158:161], v224, v149 op_sel_hi:[0,0,0]
	v_mfma_scale_f32_16x16x128_f8f6f4 v[162:165], v[12:19], v[48:55], v[162:165], v224, v149 op_sel_hi:[0,0,0]
	v_mfma_scale_f32_16x16x128_f8f6f4 v[166:169], v[4:11], v[56:63], v[166:169], v224, v149 op_sel_hi:[0,0,0]
	v_mfma_scale_f32_16x16x128_f8f6f4 v[170:173], v[12:19], v[56:63], v[170:173], v224, v149 op_sel_hi:[0,0,0]
	v_mfma_scale_f32_16x16x128_f8f6f4 v[174:177], v[4:11], v[232:239], v[174:177], v224, v149 op_sel_hi:[0,0,0]
	v_mfma_scale_f32_16x16x128_f8f6f4 v[182:185], v[12:19], v[232:239], v[182:185], v224, v149 op_sel_hi:[0,0,0]
	s_setprio 0
	s_barrier
	s_add_i32 s3, s40, s43
	v_lshl_add_u64 v[64:65], v[220:221], 0, s[38:39]
	s_mov_b32 m0, s3
	s_nop 0
	global_load_lds_dwordx4 v[64:65], off
	s_add_i32 m0, s3, 0x2000
	s_add_u32 s46, s46, 0x20080
	v_lshl_add_u64 v[64:65], v[218:219], 0, s[38:39]
	s_addc_u32 s47, s47, 0
	s_add_i32 s3, s41, s43
	global_load_lds_dwordx4 v[64:65], off
	v_lshl_add_u64 v[64:65], s[46:47], 0, v[198:199]
	s_mov_b32 m0, s3
	v_lshl_add_u64 v[36:37], v[36:37], 0, s[38:39]
	global_load_lds_dwordx4 v[64:65], off
	v_lshl_add_u64 v[64:65], s[46:47], 0, v[200:201]
	s_add_i32 m0, s3, 0x2000
	s_nop 0
	global_load_lds_dwordx4 v[64:65], off
	s_mov_b32 m0, s63
	s_nop 0
	global_load_lds_dwordx4 v[36:37], off
	v_lshl_add_u64 v[36:37], v[38:39], 0, s[38:39]
	s_mov_b32 m0, s64
	s_nop 0
	global_load_lds_dwordx4 v[36:37], off
	ds_read_b128 v[40:43], v227 offset:49152
	ds_read_b128 v[44:47], v227 offset:50176
	ds_read_b128 v[48:51], v227 offset:51200
	ds_read_b128 v[52:55], v227 offset:52224
	ds_read_b128 v[56:59], v227 offset:53248
	ds_read_b128 v[60:63], v227 offset:54272
	ds_read_b128 v[232:235], v227 offset:55296
	ds_read_b128 v[236:239], v227 offset:56320
	s_waitcnt vmcnt(8)
	s_waitcnt lgkmcnt(0)
	s_barrier
	s_setprio 1
	s_waitcnt lgkmcnt(0)
	v_mfma_scale_f32_16x16x128_f8f6f4 v[68:71], v[20:27], v[40:47], v[68:71], v224, v149 op_sel_hi:[0,0,0]
	v_mfma_scale_f32_16x16x128_f8f6f4 v[72:75], v[28:35], v[40:47], v[72:75], v224, v149 op_sel_hi:[0,0,0]
	v_mfma_scale_f32_16x16x128_f8f6f4 v[76:79], v[20:27], v[48:55], v[76:79], v224, v149 op_sel_hi:[0,0,0]
	v_mfma_scale_f32_16x16x128_f8f6f4 v[84:87], v[28:35], v[48:55], v[84:87], v224, v149 op_sel_hi:[0,0,0]
	v_mfma_scale_f32_16x16x128_f8f6f4 v[92:95], v[20:27], v[56:63], v[92:95], v224, v149 op_sel_hi:[0,0,0]
	v_mfma_scale_f32_16x16x128_f8f6f4 v[100:103], v[28:35], v[56:63], v[100:103], v224, v149 op_sel_hi:[0,0,0]
	v_mfma_scale_f32_16x16x128_f8f6f4 v[108:111], v[20:27], v[232:239], v[108:111], v224, v149 op_sel_hi:[0,0,0]
	v_mfma_scale_f32_16x16x128_f8f6f4 v[116:119], v[28:35], v[232:239], v[116:119], v224, v149 op_sel_hi:[0,0,0]
	s_setprio 0
	s_setprio 1
	v_mfma_scale_f32_16x16x128_f8f6f4 v[124:127], v[4:11], v[40:47], v[124:127], v224, v149 op_sel_hi:[0,0,0]
	v_mfma_scale_f32_16x16x128_f8f6f4 v[136:139], v[12:19], v[40:47], v[136:139], v224, v149 op_sel_hi:[0,0,0]
	v_mfma_scale_f32_16x16x128_f8f6f4 v[140:143], v[4:11], v[48:55], v[140:143], v224, v149 op_sel_hi:[0,0,0]
	v_mfma_scale_f32_16x16x128_f8f6f4 v[150:153], v[12:19], v[48:55], v[150:153], v224, v149 op_sel_hi:[0,0,0]
	v_mfma_scale_f32_16x16x128_f8f6f4 v[178:181], v[4:11], v[56:63], v[178:181], v224, v149 op_sel_hi:[0,0,0]
	v_mfma_scale_f32_16x16x128_f8f6f4 v[186:189], v[12:19], v[56:63], v[186:189], v224, v149 op_sel_hi:[0,0,0]
	v_mfma_scale_f32_16x16x128_f8f6f4 v[190:193], v[4:11], v[232:239], v[190:193], v224, v149 op_sel_hi:[0,0,0]
	v_mfma_scale_f32_16x16x128_f8f6f4 v[194:197], v[12:19], v[232:239], v[194:197], v224, v149 op_sel_hi:[0,0,0]
	s_setprio 0
	s_barrier
	s_add_i32 s73, s73, 2
	s_add_u32 s44, s44, 0x100
	s_addc_u32 s45, s45, 0
	s_cmp_gt_u32 s73, 5
	s_cbranch_scc1 .LBB0_897
.LBB0_890:
	v_lshl_add_u64 v[218:219], v[216:217], 0, s[44:45]
	s_add_i32 m0, s55, 0xc000
	s_nop 0
	global_load_lds_dwordx4 v[218:219], off
	v_lshl_add_u64 v[218:219], v[214:215], 0, s[44:45]
	s_add_i32 m0, s55, 0xe000
	s_nop 0
	global_load_lds_dwordx4 v[218:219], off
	v_add_u32_e32 v2, 0, v226
	v_add_u32_e32 v4, 0x10000, v2
	v_add_u32_e32 v2, 0x14000, v2
	ds_read_b128 v[20:23], v4
	ds_read_b128 v[24:27], v4 offset:1024
	ds_read_b128 v[28:31], v4 offset:2048
	ds_read_b128 v[32:35], v4 offset:3072
	ds_read_b128 v[4:7], v2
	ds_read_b128 v[8:11], v2 offset:1024
	ds_read_b128 v[12:15], v2 offset:2048
	ds_read_b128 v[16:19], v2 offset:3072
	ds_read_b128 v[36:39], v227
	ds_read_b128 v[40:43], v227 offset:1024
	ds_read_b128 v[44:47], v227 offset:2048
	ds_read_b128 v[48:51], v227 offset:3072
	ds_read_b128 v[52:55], v227 offset:4096
	ds_read_b128 v[56:59], v227 offset:5120
	ds_read_b128 v[60:63], v227 offset:6144
	ds_read_b128 v[64:67], v227 offset:7168
	s_cmp_lg_u32 s44, 0
	s_waitcnt vmcnt(8)
	s_waitcnt lgkmcnt(0)
	s_cselect_b64 s[50:51], -1, 0
	s_barrier
	s_setprio 1
	s_and_b64 vcc, exec, s[50:51]
	s_cbranch_vccz .LBB0_895
	s_waitcnt lgkmcnt(0)
	v_mfma_scale_f32_16x16x128_f8f6f4 v[80:83], v[20:27], v[36:43], v[80:83], v224, v149 op_sel_hi:[0,0,0]
	v_mfma_scale_f32_16x16x128_f8f6f4 v[88:91], v[28:35], v[36:43], v[88:91], v224, v149 op_sel_hi:[0,0,0]
	v_mfma_scale_f32_16x16x128_f8f6f4 v[96:99], v[20:27], v[44:51], v[96:99], v224, v149 op_sel_hi:[0,0,0]
	v_mfma_scale_f32_16x16x128_f8f6f4 v[104:107], v[28:35], v[44:51], v[104:107], v224, v149 op_sel_hi:[0,0,0]
	v_mfma_scale_f32_16x16x128_f8f6f4 v[112:115], v[20:27], v[52:59], v[112:115], v224, v149 op_sel_hi:[0,0,0]
	v_mfma_scale_f32_16x16x128_f8f6f4 v[120:123], v[28:35], v[52:59], v[120:123], v224, v149 op_sel_hi:[0,0,0]
	v_mfma_scale_f32_16x16x128_f8f6f4 v[128:131], v[20:27], v[60:67], v[128:131], v224, v149 op_sel_hi:[0,0,0]
	v_mfma_scale_f32_16x16x128_f8f6f4 v[132:135], v[28:35], v[60:67], v[132:135], v224, v149 op_sel_hi:[0,0,0]
	s_setprio 0
	s_setprio 1
	v_mfma_scale_f32_16x16x128_f8f6f4 v[144:147], v[4:11], v[36:43], v[144:147], v224, v149 op_sel_hi:[0,0,0]
	v_mfma_scale_f32_16x16x128_f8f6f4 v[154:157], v[12:19], v[36:43], v[154:157], v224, v149 op_sel_hi:[0,0,0]
	v_mfma_scale_f32_16x16x128_f8f6f4 v[158:161], v[4:11], v[44:51], v[158:161], v224, v149 op_sel_hi:[0,0,0]
	v_mfma_scale_f32_16x16x128_f8f6f4 v[162:165], v[12:19], v[44:51], v[162:165], v224, v149 op_sel_hi:[0,0,0]
	v_mfma_scale_f32_16x16x128_f8f6f4 v[166:169], v[4:11], v[52:59], v[166:169], v224, v149 op_sel_hi:[0,0,0]
	v_mfma_scale_f32_16x16x128_f8f6f4 v[170:173], v[12:19], v[52:59], v[170:173], v224, v149 op_sel_hi:[0,0,0]
	v_mfma_scale_f32_16x16x128_f8f6f4 v[174:177], v[4:11], v[60:67], v[174:177], v224, v149 op_sel_hi:[0,0,0]
	v_mfma_scale_f32_16x16x128_f8f6f4 v[182:185], v[12:19], v[60:67], v[182:185], v224, v149 op_sel_hi:[0,0,0]
	s_cbranch_execnz .LBB0_893

.LBB0_893:
	s_add_u32 s3, s6, s44
	s_addc_u32 s27, s7, s45
	s_add_u32 s3, s3, 0x58200100
	s_addc_u32 s27, s27, 0
	s_add_u32 s74, s71, s44
	s_addc_u32 s75, s72, s45
	s_cmpk_eq_i32 s44, 0x300
	s_cselect_b64 s[40:41], -1, 0
	s_and_b64 s[46:47], s[40:41], exec
	v_cndmask_b32_e64 v2, v208, v228, s[40:41]
	s_cselect_b32 s49, s11, s27
	s_cselect_b32 s48, s10, s3
	v_cndmask_b32_e64 v222, v212, v230, s[40:41]
	s_cselect_b32 s47, s21, s75
	s_cselect_b32 s46, s70, s74
	s_setprio 0
	s_barrier
	s_mov_b32 m0, s56
	v_lshl_add_u64 v[220:221], s[46:47], 0, v[198:199]
	s_add_u32 s74, s46, 0x20000
	global_load_lds_dwordx4 v[220:221], off
	v_lshl_add_u64 v[218:219], s[46:47], 0, v[200:201]
	s_mov_b32 m0, s57
	s_addc_u32 s75, s47, 0
	global_load_lds_dwordx4 v[218:219], off
	v_lshl_add_u64 v[232:233], s[74:75], 0, v[198:199]
	s_mov_b32 m0, s58
	s_nop 0
	global_load_lds_dwordx4 v[232:233], off
	v_lshl_add_u64 v[232:233], s[74:75], 0, v[200:201]
	s_mov_b32 m0, s59
	s_nop 0
	global_load_lds_dwordx4 v[232:233], off
	s_mov_b32 m0, s55
	s_nop 0
	global_load_lds_dwordx4 v2, s[48:49]
	s_mov_b32 m0, s60
	s_nop 0
	global_load_lds_dwordx4 v222, s[48:49]
	s_waitcnt lgkmcnt(0)
	ds_read_b128 v[36:39], v227 offset:16384
	ds_read_b128 v[40:43], v227 offset:17408
	ds_read_b128 v[44:47], v227 offset:18432
	ds_read_b128 v[48:51], v227 offset:19456
	ds_read_b128 v[52:55], v227 offset:20480
	ds_read_b128 v[56:59], v227 offset:21504
	ds_read_b128 v[60:63], v227 offset:22528
	ds_read_b128 v[64:67], v227 offset:23552
	s_waitcnt vmcnt(8)
	s_waitcnt lgkmcnt(0)
	s_barrier
	s_setprio 1
	s_and_b64 vcc, exec, s[50:51]
	s_cbranch_vccz .LBB0_896
	s_waitcnt lgkmcnt(0)
	v_mfma_scale_f32_16x16x128_f8f6f4 v[68:71], v[20:27], v[36:43], v[68:71], v224, v149 op_sel_hi:[0,0,0]
	v_mfma_scale_f32_16x16x128_f8f6f4 v[72:75], v[28:35], v[36:43], v[72:75], v224, v149 op_sel_hi:[0,0,0]
	v_mfma_scale_f32_16x16x128_f8f6f4 v[76:79], v[20:27], v[44:51], v[76:79], v224, v149 op_sel_hi:[0,0,0]
	v_mfma_scale_f32_16x16x128_f8f6f4 v[84:87], v[28:35], v[44:51], v[84:87], v224, v149 op_sel_hi:[0,0,0]
	v_mfma_scale_f32_16x16x128_f8f6f4 v[92:95], v[20:27], v[52:59], v[92:95], v224, v149 op_sel_hi:[0,0,0]
	v_mfma_scale_f32_16x16x128_f8f6f4 v[100:103], v[28:35], v[52:59], v[100:103], v224, v149 op_sel_hi:[0,0,0]
	v_mfma_scale_f32_16x16x128_f8f6f4 v[108:111], v[20:27], v[60:67], v[108:111], v224, v149 op_sel_hi:[0,0,0]
	v_mfma_scale_f32_16x16x128_f8f6f4 v[116:119], v[28:35], v[60:67], v[116:119], v224, v149 op_sel_hi:[0,0,0]
	s_setprio 0
	s_setprio 1
	v_mfma_scale_f32_16x16x128_f8f6f4 v[124:127], v[4:11], v[36:43], v[124:127], v224, v149 op_sel_hi:[0,0,0]
	v_mfma_scale_f32_16x16x128_f8f6f4 v[136:139], v[12:19], v[36:43], v[136:139], v224, v149 op_sel_hi:[0,0,0]
	v_mfma_scale_f32_16x16x128_f8f6f4 v[140:143], v[4:11], v[44:51], v[140:143], v224, v149 op_sel_hi:[0,0,0]
	v_mfma_scale_f32_16x16x128_f8f6f4 v[150:153], v[12:19], v[44:51], v[150:153], v224, v149 op_sel_hi:[0,0,0]
	v_mfma_scale_f32_16x16x128_f8f6f4 v[178:181], v[4:11], v[52:59], v[178:181], v224, v149 op_sel_hi:[0,0,0]
	v_mfma_scale_f32_16x16x128_f8f6f4 v[186:189], v[12:19], v[52:59], v[186:189], v224, v149 op_sel_hi:[0,0,0]
	v_mfma_scale_f32_16x16x128_f8f6f4 v[190:193], v[4:11], v[60:67], v[190:193], v224, v149 op_sel_hi:[0,0,0]
	v_mfma_scale_f32_16x16x128_f8f6f4 v[194:197], v[12:19], v[60:67], v[194:197], v224, v149 op_sel_hi:[0,0,0]
	s_cbranch_execnz .LBB0_889
	s_branch .LBB0_888
